# speedup vs baseline: 1.0148x; 1.0148x over previous
_Z11proj_kernelPKfPKDv8_DF16_PDF16_S4_S4_:
	v_mov_b32_e32 v164, 0x20000
	v_mov_b32_e32 v172, 0
	v_mov_b32_e32 v173, 0
	v_mov_b32_e32 v174, 0
	v_mov_b32_e32 v175, 0
	v_mov_b32_e32 v171, 0
	v_lshrrev_b32_e32 v169, 6, v0
	v_lshlrev_b32_e32 v169, 2, v169
	v_add_u32_e32 v169, 0x1fff0, v169
	ds_write_b128 v164, v[172:175]
	v_readfirstlane_b32 s13, v0
	s_lshl_b32 s12, s2, 6
	s_lshr_b32 s3, s2, 3
	s_cmpk_lt_u32 s13, 0x100
	v_and_b32_e32 v1, 15, v0
	s_mov_b64 s[4:5], -1
	s_cbranch_scc1 .LBB1_3
	s_andn2_b64 vcc, exec, s[4:5]
	s_cbranch_vccz .LBB1_4

.LBB1_3:
	s_load_dwordx8 s[4:11], s[0:1], 0x8
	s_lshr_b32 s16, s13, 6
	s_mul_i32 s14, s16, 0x1800
	s_mov_b32 s15, 0
	s_lshl_b64 s[18:19], s[14:15], 4
	v_and_b32_e32 v2, 63, v0
	s_waitcnt lgkmcnt(0)
	s_lshl_b32 s24, s12, 7
	s_add_u32 s21, s6, s24
	s_add_u32 s22, s8, s24
	s_add_u32 s23, s10, s24
	s_sub_u32 s21, s21, 0x20100
	s_sub_u32 s22, s22, 0x22100
	s_sub_u32 s23, s23, 0x24100
	s_add_u32 s4, s4, s18
	s_addc_u32 s5, s5, s19
	v_lshlrev_b32_e32 v54, 4, v2
	v_mov_b32_e32 v55, 0
	v_lshl_add_u64 v[18:19], s[4:5], 0, v[54:55]
	s_bfe_u32 s4, s2, 0x40003
	s_mul_i32 s14, s4, 0x1800
	v_lshl_add_u64 v[20:21], v[18:19], 0, s[14:15]
	global_load_dwordx4 v[2:5], v[20:21], off offset:2048
	global_load_dwordx4 v[6:9], v[20:21], off
	global_load_dwordx4 v[10:13], v[20:21], off offset:1024
	v_lshrrev_b32_e32 v14, 1, v0
	v_bfe_u32 v56, v0, 4, 2
	v_lshlrev_b32_e32 v54, 7, v1
	v_bitop3_b32 v14, v56, v14, 7 bitop3:0x78
	v_lshl_or_b32 v57, v14, 4, v54
	global_load_dwordx4 v[14:17], v[20:21], off offset:3072
	s_movk_i32 s2, 0x1000
	s_add_i32 s5, s3, 1
	s_and_b32 s5, s5, 15
	v_add_co_u32_e32 v44, vcc, s2, v20
	s_mul_i32 s14, s5, 0x1800
	s_nop 0
	v_addc_co_u32_e32 v45, vcc, 0, v21, vcc
	v_lshl_add_u64 v[46:47], v[18:19], 0, s[14:15]
	global_load_dwordx4 v[20:23], v[44:45], off
	global_load_dwordx4 v[24:27], v[44:45], off offset:1024
	global_load_dwordx4 v[28:31], v[46:47], off
	global_load_dwordx4 v[32:35], v[46:47], off offset:1024
	global_load_dwordx4 v[36:39], v[46:47], off offset:2048
	global_load_dwordx4 v[40:43], v[46:47], off offset:3072
	s_add_i32 s13, s3, 2
	s_and_b32 s13, s13, 15
	v_add_co_u32_e32 v52, vcc, s2, v46
	s_mul_i32 s14, s13, 0x1800
	s_nop 0
	v_addc_co_u32_e32 v53, vcc, 0, v47, vcc
	v_lshl_add_u64 v[58:59], v[18:19], 0, s[14:15]
	global_load_dwordx4 v[44:47], v[52:53], off
	global_load_dwordx4 v[48:51], v[52:53], off offset:1024
	global_load_dwordx4 v[60:63], v[58:59], off
	global_load_dwordx4 v[64:67], v[58:59], off offset:1024
	global_load_dwordx4 v[68:71], v[58:59], off offset:2048
	global_load_dwordx4 v[72:75], v[58:59], off offset:3072
	v_add_co_u32_e32 v52, vcc, s2, v58
	s_add_i32 s5, s3, 3
	s_nop 0
	v_addc_co_u32_e32 v53, vcc, 0, v59, vcc
	global_load_dwordx4 v[76:79], v[52:53], off
	global_load_dwordx4 v[80:83], v[52:53], off offset:1024
	s_waitcnt lgkmcnt(0)
	s_barrier

.Lproj_go_15:
	s_waitcnt vmcnt(8)
	v_mfma_f32_16x16x32_f16 v[100:103], v[10:13], v[116:119], v[100:103]
	ds_read_b128 v[128:131], v59
	ds_read_b128 v[132:135], v132
	v_or_b32_e32 v59, 0x1f000, v57
	v_or_b32_e32 v57, 0x1f800, v57
	s_waitcnt vmcnt(7)
	v_mfma_f32_16x16x32_f16 v[104:107], v[6:9], v[116:119], v[104:107]
	ds_read_b128 v[136:139], v59
	ds_read_b128 v[140:143], v57
	v_or_b32_e32 v57, 0x1e000, v58
	v_or_b32_e32 v59, 0x1e800, v58
	s_waitcnt vmcnt(6)
	v_mfma_f32_16x16x32_f16 v[68:71], v[116:119], v[2:5], v[68:71]
	ds_read_b128 v[116:119], v57
	ds_read_b128 v[144:147], v59
	v_or_b32_e32 v57, 0x1f000, v58
	v_or_b32_e32 v58, 0x1f800, v58
	s_waitcnt vmcnt(5) lgkmcnt(5)
	v_mfma_f32_16x16x32_f16 v[100:103], v[38:41], v[128:131], v[100:103]
	ds_read_b128 v[148:151], v57
	ds_read_b128 v[152:155], v58
	v_lshl_add_u64 v[58:59], s[4:5], 0, v[54:55]
	v_and_b32_e32 v54, 48, v0
	s_waitcnt vmcnt(4)
	v_mfma_f32_16x16x32_f16 v[104:107], v[34:37], v[128:131], v[104:107]
	s_lshl_b32 s4, s16, 5
	s_waitcnt vmcnt(3)
	v_mfma_f32_16x16x32_f16 v[68:71], v[128:131], v[30:33], v[68:71]
	v_lshl_add_u64 v[128:129], v[58:59], 0, v[54:55]
	s_waitcnt vmcnt(2) lgkmcnt(3)
	v_mfma_f32_16x16x32_f16 v[100:103], v[22:25], v[116:119], v[100:103]
	s_waitcnt vmcnt(1)
	v_mfma_f32_16x16x32_f16 v[104:107], v[26:29], v[116:119], v[104:107]
	s_waitcnt vmcnt(0)
	v_mfma_f32_16x16x32_f16 v[68:71], v[116:119], v[18:21], v[68:71]
	s_nop 3
	v_mov_b32_e32 v54, v101
	v_mov_b32_e32 v55, v102
	v_mul_f32_e64 v54, v54, s2
	v_mul_f32_e64 v55, v55, s2
	v_mfma_f32_16x16x32_f16 v[76:79], v[10:13], v[120:123], v[76:79]
	v_fma_mixlo_f16 v57, v100, s2, 0
	v_cvt_pk_f16_f32 v100, v54, v55
	v_mov_b32_e32 v54, v105
	v_mov_b32_e32 v55, v106
	v_mfma_f32_16x16x32_f16 v[84:87], v[6:9], v[120:123], v[84:87]
	v_mul_f32_e64 v54, v54, s2
	v_mul_f32_e64 v55, v55, s2
	v_pack_b32_f16 v58, v57, v100
	v_cvt_pk_f16_f32 v57, v54, v55
	v_mov_b32_e32 v54, v69
	v_mfma_f32_16x16x32_f16 v[88:91], v[120:123], v[2:5], v[88:91]
	v_mov_b32_e32 v55, v70
	v_mul_f32_e64 v54, v54, s2
	v_mul_f32_e64 v55, v55, s2
	v_fma_mixlo_f16 v59, v104, s2, 0
	v_mfma_f32_16x16x32_f16 v[76:79], v[38:41], v[132:135], v[76:79]
	v_cvt_pk_f16_f32 v70, v54, v55
	v_fma_mixlo_f16 v54, v103, s2, 0
	v_fma_mixlo_f16 v104, v68, s2, 0
	v_mfma_f32_16x16x32_f16 v[84:87], v[34:37], v[132:135], v[84:87]
	v_pack_b32_f16 v68, v59, v57
	v_alignbit_b32 v59, v54, v100, 16
	v_fma_mixlo_f16 v54, v107, s2, 0
	v_alignbit_b32 v69, v54, v57, 16
	v_lshlrev_b64 v[100:101], 7, v[156:157]
	v_mfma_f32_16x16x32_f16 v[88:91], v[132:135], v[30:33], v[88:91]
	v_lshl_or_b32 v105, v56, 3, s4
	v_or_b32_e32 v100, v100, v105
	v_lshl_add_u64 v[102:103], s[6:7], 0, v[100:101]
	s_waitcnt lgkmcnt(2)
	v_mfma_f32_16x16x32_f16 v[54:57], v[22:25], v[144:147], v[76:79]
	v_subrev_u32_e32 v170, s21, v102
	ds_write_b64 v170, v[58:59]
	v_lshl_add_u64 v[58:59], s[8:9], 0, v[100:101]
	v_subrev_u32_e32 v170, s22, v58
	ds_write_b64 v170, v[68:69]
	v_mfma_f32_16x16x32_f16 v[76:79], v[26:29], v[144:147], v[84:87]
	v_or_b32_e32 v68, 16, v156
	s_nop 2
	v_fma_mixlo_f16 v58, v54, s2, 0
	v_mov_b32_e32 v54, v55
	v_mfma_f32_16x16x32_f16 v[84:87], v[144:147], v[18:21], v[88:91]
	v_mov_b32_e32 v55, v56
	v_mul_f32_e64 v54, v54, s2
	v_mul_f32_e64 v55, v55, s2
	v_fma_mixlo_f16 v59, v76, s2, 0
	v_mfma_f32_16x16x32_f16 v[60:63], v[46:49], v[80:83], v[60:63]
	v_cvt_pk_f16_f32 v56, v54, v55
	v_mov_b32_e32 v54, v77
	v_mov_b32_e32 v55, v78
	v_mfma_f32_16x16x32_f16 v[72:75], v[42:45], v[80:83], v[72:75]
	v_mul_f32_e64 v54, v54, s2
	v_mul_f32_e64 v55, v55, s2
	v_pack_b32_f16 v76, v58, v56
	v_ashrrev_i32_e32 v69, 31, v68
	v_mfma_f32_16x16x32_f16 v[80:83], v[80:83], v[14:17], v[92:95]
	v_lshlrev_b64 v[68:69], 7, v[68:69]
	v_or_b32_e32 v68, v68, v105
	v_fma_mixlo_f16 v84, v84, s2, 0
	v_mfma_f32_16x16x32_f16 v[42:45], v[42:45], v[112:115], v[64:67]
	s_nop 2
	v_cvt_pk_f16_f32 v67, v54, v55
	v_mov_b32_e32 v54, v85
	v_mov_b32_e32 v55, v86
	v_mul_f32_e64 v54, v54, s2
	v_mul_f32_e64 v55, v55, s2
	v_pack_b32_f16 v66, v59, v67
	v_mfma_f32_16x16x32_f16 v[58:61], v[10:13], v[96:99], v[60:63]
	v_mfma_f32_16x16x32_f16 v[62:65], v[6:9], v[96:99], v[72:75]
	s_nop 2
	v_cvt_pk_f16_f32 v74, v54, v55
	v_fma_mixlo_f16 v54, v57, s2, 0
	v_alignbit_b32 v77, v54, v56, 16
	v_mfma_f32_16x16x32_f16 v[54:57], v[96:99], v[2:5], v[80:83]
	v_fma_mixlo_f16 v72, v79, s2, 0
	v_alignbit_b32 v67, v72, v67, 16
	v_lshl_add_u64 v[72:73], s[6:7], 0, v[68:69]
	v_mfma_f32_16x16x32_f16 v[46:49], v[46:49], v[112:115], v[108:111]
	v_lshl_add_u64 v[68:69], s[8:9], 0, v[68:69]
	v_subrev_u32_e32 v170, s22, v68
	ds_write_b64 v170, v[66:67]
	v_lshrrev_b32_e32 v67, 16, v70
	v_mfma_f32_16x16x32_f16 v[58:61], v[38:41], v[136:139], v[58:61]
	v_lshrrev_b32_e32 v69, 16, v74
	v_fma_mixhi_f16 v69, v87, s2, 0
	v_fma_mixhi_f16 v67, v71, s2, 0
	v_mfma_f32_16x16x32_f16 v[54:57], v[136:139], v[30:33], v[54:57]
	v_pack_b32_f16 v68, v84, v74
	v_pack_b32_f16 v66, v104, v70
	v_subrev_u32_e32 v170, s23, v128
	ds_write_b128 v170, v[66:69]
	v_mfma_f32_16x16x32_f16 v[62:65], v[34:37], v[136:139], v[62:65]
	v_subrev_u32_e32 v170, s21, v72
	ds_write_b64 v170, v[76:77]
	v_or_b32_e32 v66, 32, v156
	v_ashrrev_i32_e32 v67, 31, v66
	v_mfma_f32_16x16x32_f16 v[14:17], v[112:115], v[14:17], v[50:53]
	v_mfma_f32_16x16x32_f16 v[6:9], v[6:9], v[124:127], v[42:45]
	s_waitcnt lgkmcnt(1)
	v_mfma_f32_16x16x32_f16 v[58:61], v[22:25], v[148:151], v[58:61]
	v_mfma_f32_16x16x32_f16 v[54:57], v[148:151], v[18:21], v[54:57]
	v_mfma_f32_16x16x32_f16 v[10:13], v[10:13], v[124:127], v[46:49]
	s_nop 5
	v_fma_mixlo_f16 v68, v58, s2, 0
	v_mov_b32_e32 v58, v59
	v_mov_b32_e32 v59, v60
	v_mfma_f32_16x16x32_f16 v[62:65], v[26:29], v[148:151], v[62:65]
	v_mul_f32_e64 v50, v58, s2
	v_mul_f32_e64 v51, v59, s2
	v_fma_mixlo_f16 v54, v54, s2, 0
	v_cvt_pk_f16_f32 v50, v50, v51
	v_mfma_f32_16x16x32_f16 v[2:5], v[124:127], v[2:5], v[14:17]
	v_pack_b32_f16 v46, v68, v50
	s_nop 1
	v_mov_b32_e32 v48, v63
	v_mov_b32_e32 v49, v64
	v_mfma_f32_16x16x32_f16 v[6:9], v[34:37], v[140:143], v[6:9]
	v_mov_b32_e32 v14, v55
	v_mov_b32_e32 v15, v56
	v_mul_f32_e64 v14, v14, s2
	v_mul_f32_e64 v15, v15, s2
	v_mfma_f32_16x16x32_f16 v[10:13], v[38:41], v[140:143], v[10:13]
	v_mul_f32_e64 v42, v48, s2
	v_mul_f32_e64 v43, v49, s2
	v_cvt_pk_f16_f32 v38, v14, v15
	v_fma_mixlo_f16 v14, v61, s2, 0
	v_mfma_f32_16x16x32_f16 v[2:5], v[140:143], v[30:33], v[2:5]
	v_fma_mixlo_f16 v62, v62, s2, 0
	v_cvt_pk_f16_f32 v43, v42, v43
	v_alignbit_b32 v47, v14, v50, 16
	v_fma_mixlo_f16 v14, v65, s2, 0
	s_waitcnt lgkmcnt(0)
	v_mfma_f32_16x16x32_f16 v[6:9], v[26:29], v[152:155], v[6:9]
	v_pack_b32_f16 v42, v62, v43
	v_alignbit_b32 v43, v14, v43, 16
	v_lshlrev_b64 v[14:15], 7, v[66:67]
	v_mfma_f32_16x16x32_f16 v[10:13], v[22:25], v[152:155], v[10:13]
	v_or_b32_e32 v14, v14, v105
	v_lshl_add_u64 v[16:17], s[6:7], 0, v[14:15]
	v_subrev_u32_e32 v170, s21, v16
	ds_write_b64 v170, v[46:47]
	v_mfma_f32_16x16x32_f16 v[2:5], v[152:155], v[18:21], v[2:5]
	v_lshl_add_u64 v[14:15], s[8:9], 0, v[14:15]
	v_fma_mixlo_f16 v17, v6, s2, 0
	v_mov_b32_e32 v6, v7
	v_mov_b32_e32 v7, v8
	v_subrev_u32_e32 v170, s22, v14
	ds_write_b64 v170, v[42:43]
	v_or_b32_e32 v14, 48, v156
	v_fma_mixlo_f16 v16, v10, s2, 0
	v_mov_b32_e32 v10, v11
	v_mov_b32_e32 v11, v12
	v_mul_f32_e64 v6, v6, s2
	v_mul_f32_e64 v7, v7, s2
	v_ashrrev_i32_e32 v15, 31, v14
	v_mul_f32_e64 v10, v10, s2
	v_mul_f32_e64 v11, v11, s2
	v_cvt_pk_f16_f32 v7, v6, v7
	v_fma_mixlo_f16 v8, v9, s2, 0
	v_cvt_pk_f16_f32 v12, v10, v11
	v_pack_b32_f16 v6, v17, v7
	v_mov_b32_e32 v10, v3
	v_mov_b32_e32 v11, v4
	v_alignbit_b32 v7, v8, v7, 16
	v_lshlrev_b64 v[8:9], 7, v[14:15]
	v_mul_f32_e64 v10, v10, s2
	v_mul_f32_e64 v11, v11, s2
	v_fma_mixlo_f16 v3, v13, s2, 0
	v_or_b32_e32 v8, v8, v105
	v_fma_mixlo_f16 v18, v2, s2, 0
	v_pack_b32_f16 v2, v16, v12
	v_cvt_pk_f16_f32 v4, v10, v11
	v_alignbit_b32 v3, v3, v12, 16
	v_lshl_add_u64 v[10:11], s[6:7], 0, v[8:9]
	v_subrev_u32_e32 v170, s21, v10
	ds_write_b64 v170, v[2:3]
	v_lshl_add_u64 v[2:3], s[8:9], 0, v[8:9]
	v_subrev_u32_e32 v170, s22, v2
	ds_write_b64 v170, v[6:7]
	v_lshrrev_b32_e32 v7, 16, v38
	v_lshrrev_b32_e32 v9, 16, v4
	v_fma_mixhi_f16 v9, v5, s2, 0
	v_fma_mixhi_f16 v7, v57, s2, 0
	v_pack_b32_f16 v8, v18, v4
	v_pack_b32_f16 v6, v54, v38
	v_subrev_u32_e32 v170, s23, v128
	ds_write_b128 v170, v[6:9] offset:64
	s_waitcnt lgkmcnt(0)
	s_barrier
	v_and_b32_e32 v170, 63, v0
	v_lshlrev_b32_e32 v170, 4, v170
	v_lshl_add_u32 v170, s16, 10, v170
	v_add_u32_e32 v168, s24, v170
	v_add_u32_e32 v169, 0x1000, v168
	v_add_u32_e32 v170, 0x20100, v170
	ds_read_b128 v[160:163], v170
	ds_read_b128 v[164:167], v170 offset:4096
	ds_read_b128 v[172:175], v170 offset:8192
	s_waitcnt lgkmcnt(2)
	global_store_dwordx4 v168, v[160:163], s[6:7] sc1
	s_waitcnt lgkmcnt(1)
	global_store_dwordx4 v169, v[164:167], s[6:7] sc1
	s_waitcnt lgkmcnt(0)
	global_store_dwordx4 v168, v[172:175], s[8:9] sc1
	s_nop 1
	ds_read_b128 v[160:163], v170 offset:12288
	ds_read_b128 v[164:167], v170 offset:16384
	ds_read_b128 v[172:175], v170 offset:20480
	s_waitcnt lgkmcnt(2)
	global_store_dwordx4 v169, v[160:163], s[8:9] sc1
	s_waitcnt lgkmcnt(1)
	global_store_dwordx4 v168, v[164:167], s[10:11] sc1
	s_waitcnt lgkmcnt(0)
	global_store_dwordx4 v169, v[172:175], s[10:11] sc1
	s_endpgm
.LBB1_4:
	s_load_dwordx2 s[0:1], s[0:1], 0x0
	v_add_u32_e32 v2, 0xffffff00, v0
	v_ashrrev_i32_e32 v20, 4, v2
	v_add_u32_e32 v2, s12, v20
	v_ashrrev_i32_e32 v3, 31, v2
	v_lshlrev_b64 v[2:3], 12, v[2:3]
	s_lshl_b32 s2, s3, 6
	s_waitcnt lgkmcnt(0)
	v_lshl_add_u64 v[2:3], s[0:1], 0, v[2:3]
	v_lshlrev_b32_e32 v4, 4, v1
	v_mov_b32_e32 v5, 0
	s_and_b32 s6, s2, 0x3c0
	s_mov_b32 s1, 0
	v_lshl_add_u64 v[2:3], v[2:3], 0, v[4:5]
	s_lshl_b32 s0, s6, 2
	v_lshl_add_u64 v[16:17], v[2:3], 0, s[0:1]
	s_mov_b32 s3, 0x10000
	v_add_co_u32_e32 v12, vcc, s3, v16
	s_mov_b32 s4, 0x20000
	s_nop 0
	v_addc_co_u32_e32 v13, vcc, 0, v17, vcc
	global_load_dwordx4 v[4:7], v[16:17], off sc0 sc1 nt
	global_load_dwordx4 v[8:11], v[12:13], off sc0 sc1 nt
	v_add_co_u32_e32 v12, vcc, s4, v16
	s_mov_b32 s5, 0x30000
	s_nop 0
	v_addc_co_u32_e32 v13, vcc, 0, v17, vcc
	s_add_i32 s0, s2, 64
	global_load_dwordx4 v[12:15], v[12:13], off sc0 sc1 nt
	v_add_co_u32_e32 v16, vcc, s5, v16
	s_and_b32 s0, s0, 0x3c0
	s_nop 0
	v_addc_co_u32_e32 v17, vcc, 0, v17, vcc
	s_lshl_b32 s0, s0, 2
	global_load_dwordx4 v[16:19], v[16:17], off sc0 sc1 nt
	v_lshl_add_u64 v[28:29], v[2:3], 0, s[0:1]
	v_lshrrev_b32_e32 v1, 1, v1
	v_lshrrev_b32_e32 v21, 5, v0
	v_lshlrev_b32_e32 v0, 3, v0
	v_add_co_u32_e32 v30, vcc, s3, v28
	v_bitop3_b32 v1, v1, v21, 7 bitop3:0x78
	v_and_b32_e32 v0, 8, v0
	v_addc_co_u32_e32 v31, vcc, 0, v29, vcc
	v_lshl_or_b32 v0, v1, 4, v0
	v_add_co_u32_e32 v36, vcc, s4, v28
	v_lshl_or_b32 v0, v20, 7, v0
	global_load_dwordx4 v[20:23], v[28:29], off sc0 sc1 nt
	global_load_dwordx4 v[24:27], v[30:31], off sc0 sc1 nt
	v_addc_co_u32_e32 v37, vcc, 0, v29, vcc
	s_add_i32 s0, s2, 0x80
	v_add_co_u32_e32 v38, vcc, s5, v28
	s_and_b32 s0, s0, 0x3c0
	s_nop 0
	v_addc_co_u32_e32 v39, vcc, 0, v29, vcc
	global_load_dwordx4 v[28:31], v[36:37], off sc0 sc1 nt
	global_load_dwordx4 v[32:35], v[38:39], off sc0 sc1 nt
	s_lshl_b32 s0, s0, 2
	v_lshl_add_u64 v[44:45], v[2:3], 0, s[0:1]
	v_add_co_u32_e32 v46, vcc, s3, v44
	s_add_i32 s0, s2, 0xc0
	s_nop 0
	v_addc_co_u32_e32 v47, vcc, 0, v45, vcc
	v_add_co_u32_e32 v52, vcc, s4, v44
	global_load_dwordx4 v[36:39], v[44:45], off sc0 sc1 nt
	global_load_dwordx4 v[40:43], v[46:47], off sc0 sc1 nt
	v_addc_co_u32_e32 v53, vcc, 0, v45, vcc
	v_add_co_u32_e32 v54, vcc, s5, v44
	s_and_b32 s0, s0, 0x3c0
	s_nop 0
	v_addc_co_u32_e32 v55, vcc, 0, v45, vcc
	global_load_dwordx4 v[44:47], v[52:53], off sc0 sc1 nt
	global_load_dwordx4 v[48:51], v[54:55], off sc0 sc1 nt
	s_lshl_b32 s0, s0, 2
	v_lshl_add_u64 v[60:61], v[2:3], 0, s[0:1]
	v_add_co_u32_e32 v62, vcc, s3, v60
	s_add_i32 s0, s2, 0x100
	s_nop 0
	v_addc_co_u32_e32 v63, vcc, 0, v61, vcc
	v_add_co_u32_e32 v68, vcc, s4, v60
	global_load_dwordx4 v[52:55], v[60:61], off sc0 sc1 nt
	global_load_dwordx4 v[56:59], v[62:63], off sc0 sc1 nt
	v_addc_co_u32_e32 v69, vcc, 0, v61, vcc
	v_add_co_u32_e32 v70, vcc, s5, v60
	s_and_b32 s0, s0, 0x3c0
	s_nop 0
	v_addc_co_u32_e32 v71, vcc, 0, v61, vcc
	global_load_dwordx4 v[60:63], v[68:69], off sc0 sc1 nt
	global_load_dwordx4 v[64:67], v[70:71], off sc0 sc1 nt
	s_lshl_b32 s0, s0, 2
	v_add_u32_e32 v1, 0x10000, v0
	s_waitcnt vmcnt(15)
	v_cvt_pk_f16_f32 v7, v6, v7
	v_cvt_pk_f16_f32 v6, v4, v5
	s_waitcnt vmcnt(14)
	v_cvt_pk_f16_f32 v5, v10, v11
	v_cvt_pk_f16_f32 v4, v8, v9
	ds_write2st64_b64 v0, v[6:7], v[4:5] offset1:4
	s_waitcnt vmcnt(13)
	v_cvt_pk_f16_f32 v4, v12, v13
	v_lshl_add_u64 v[12:13], v[2:3], 0, s[0:1]
	v_cvt_pk_f16_f32 v5, v14, v15
	v_add_co_u32_e32 v14, vcc, s3, v12
	s_add_i32 s0, s2, 0x140
	s_nop 0
	v_addc_co_u32_e32 v15, vcc, 0, v13, vcc
	s_waitcnt vmcnt(12)
	v_cvt_pk_f16_f32 v7, v18, v19
	v_cvt_pk_f16_f32 v6, v16, v17
	ds_write2st64_b64 v0, v[4:5], v[6:7] offset0:8 offset1:12
	v_add_co_u32_e32 v68, vcc, s4, v12
	global_load_dwordx4 v[4:7], v[12:13], off sc0 sc1 nt
	global_load_dwordx4 v[8:11], v[14:15], off sc0 sc1 nt
	v_addc_co_u32_e32 v69, vcc, 0, v13, vcc
	v_add_co_u32_e32 v70, vcc, s5, v12
	s_and_b32 s0, s0, 0x3c0
	s_nop 0
	v_addc_co_u32_e32 v71, vcc, 0, v13, vcc
	global_load_dwordx4 v[12:15], v[68:69], off sc0 sc1 nt
	global_load_dwordx4 v[16:19], v[70:71], off sc0 sc1 nt
	s_waitcnt vmcnt(15)
	v_cvt_pk_f16_f32 v23, v22, v23
	v_cvt_pk_f16_f32 v22, v20, v21
	s_waitcnt vmcnt(14)
	v_cvt_pk_f16_f32 v21, v26, v27
	v_cvt_pk_f16_f32 v20, v24, v25
	s_lshl_b32 s0, s0, 2
	s_waitcnt lgkmcnt(0)
	s_barrier
	v_add_u32_e32 v171, 1, v171
	ds_write_b32 v169, v171
	ds_write2st64_b64 v0, v[22:23], v[20:21] offset0:16 offset1:20
	s_waitcnt vmcnt(13)
	v_cvt_pk_f16_f32 v20, v28, v29
	v_lshl_add_u64 v[28:29], v[2:3], 0, s[0:1]
	v_cvt_pk_f16_f32 v21, v30, v31
	v_add_co_u32_e32 v30, vcc, s3, v28
	s_waitcnt vmcnt(12)
	v_cvt_pk_f16_f32 v23, v34, v35
	v_cvt_pk_f16_f32 v22, v32, v33
	v_addc_co_u32_e32 v31, vcc, 0, v29, vcc
	ds_write2st64_b64 v0, v[20:21], v[22:23] offset0:24 offset1:28
	v_add_co_u32_e32 v68, vcc, s4, v28
	global_load_dwordx4 v[20:23], v[28:29], off sc0 sc1 nt
	global_load_dwordx4 v[24:27], v[30:31], off sc0 sc1 nt
	v_addc_co_u32_e32 v69, vcc, 0, v29, vcc
	s_add_i32 s0, s2, 0x180
	v_add_co_u32_e32 v70, vcc, s5, v28
	s_and_b32 s0, s0, 0x3c0
	s_nop 0
	v_addc_co_u32_e32 v71, vcc, 0, v29, vcc
	global_load_dwordx4 v[28:31], v[68:69], off sc0 sc1 nt
	global_load_dwordx4 v[32:35], v[70:71], off sc0 sc1 nt
	s_waitcnt vmcnt(15)
	v_cvt_pk_f16_f32 v39, v38, v39
	v_cvt_pk_f16_f32 v38, v36, v37
	s_waitcnt vmcnt(14)
	v_cvt_pk_f16_f32 v37, v42, v43
	v_cvt_pk_f16_f32 v36, v40, v41
	s_lshl_b32 s0, s0, 2
	s_waitcnt lgkmcnt(0)
	v_add_u32_e32 v171, 1, v171
	ds_write_b32 v169, v171
	ds_write2st64_b64 v0, v[38:39], v[36:37] offset0:32 offset1:36
	s_waitcnt vmcnt(13)
	v_cvt_pk_f16_f32 v36, v44, v45
	v_lshl_add_u64 v[44:45], v[2:3], 0, s[0:1]
	v_cvt_pk_f16_f32 v37, v46, v47
	v_add_co_u32_e32 v46, vcc, s3, v44
	s_waitcnt vmcnt(12)
	v_cvt_pk_f16_f32 v39, v50, v51
	v_cvt_pk_f16_f32 v38, v48, v49
	v_addc_co_u32_e32 v47, vcc, 0, v45, vcc
	ds_write2st64_b64 v0, v[36:37], v[38:39] offset0:40 offset1:44
	v_add_co_u32_e32 v68, vcc, s4, v44
	global_load_dwordx4 v[36:39], v[44:45], off sc0 sc1 nt
	global_load_dwordx4 v[40:43], v[46:47], off sc0 sc1 nt
	v_addc_co_u32_e32 v69, vcc, 0, v45, vcc
	v_add_co_u32_e32 v70, vcc, s5, v44
	s_add_i32 s0, s2, 0x1c0
	s_nop 0
	v_addc_co_u32_e32 v71, vcc, 0, v45, vcc
	global_load_dwordx4 v[44:47], v[68:69], off sc0 sc1 nt
	global_load_dwordx4 v[48:51], v[70:71], off sc0 sc1 nt
	s_and_b32 s0, s0, 0x3c0
	s_waitcnt vmcnt(15)
	v_cvt_pk_f16_f32 v55, v54, v55
	v_cvt_pk_f16_f32 v54, v52, v53
	s_waitcnt vmcnt(14)
	v_cvt_pk_f16_f32 v53, v58, v59
	v_cvt_pk_f16_f32 v52, v56, v57
	s_lshl_b32 s0, s0, 2
	s_waitcnt lgkmcnt(0)
	v_add_u32_e32 v171, 1, v171
	ds_write_b32 v169, v171
	ds_write2st64_b64 v0, v[54:55], v[52:53] offset0:48 offset1:52
	s_waitcnt vmcnt(13)
	v_cvt_pk_f16_f32 v52, v60, v61
	v_lshl_add_u64 v[60:61], v[2:3], 0, s[0:1]
	v_cvt_pk_f16_f32 v53, v62, v63
	v_add_co_u32_e32 v62, vcc, s3, v60
	s_waitcnt vmcnt(12)
	v_cvt_pk_f16_f32 v55, v66, v67
	v_addc_co_u32_e32 v63, vcc, 0, v61, vcc
	v_cvt_pk_f16_f32 v54, v64, v65
	v_add_co_u32_e32 v68, vcc, s4, v60
	ds_write2st64_b64 v0, v[52:53], v[54:55] offset0:56 offset1:60
	s_nop 0
	v_addc_co_u32_e32 v69, vcc, 0, v61, vcc
	global_load_dwordx4 v[52:55], v[60:61], off sc0 sc1 nt
	global_load_dwordx4 v[56:59], v[62:63], off sc0 sc1 nt
	v_add_co_u32_e32 v70, vcc, s5, v60
	s_xor_b32 s0, s6, 0x200
	s_nop 0
	v_addc_co_u32_e32 v71, vcc, 0, v61, vcc
	global_load_dwordx4 v[60:63], v[68:69], off sc0 sc1 nt
	global_load_dwordx4 v[64:67], v[70:71], off sc0 sc1 nt
	s_waitcnt vmcnt(15)
	v_cvt_pk_f16_f32 v7, v6, v7
	v_cvt_pk_f16_f32 v6, v4, v5
	s_waitcnt vmcnt(14)
	v_cvt_pk_f16_f32 v5, v10, v11
	v_cvt_pk_f16_f32 v4, v8, v9
	s_lshl_b32 s0, s0, 2
	s_waitcnt lgkmcnt(0)
	v_add_u32_e32 v171, 1, v171
	ds_write_b32 v169, v171
	ds_write2st64_b64 v0, v[6:7], v[4:5] offset0:64 offset1:68
	s_waitcnt vmcnt(13)
	v_cvt_pk_f16_f32 v4, v12, v13
	v_lshl_add_u64 v[12:13], v[2:3], 0, s[0:1]
	v_cvt_pk_f16_f32 v5, v14, v15
	v_add_co_u32_e32 v14, vcc, s3, v12
	s_waitcnt vmcnt(12)
	v_cvt_pk_f16_f32 v7, v18, v19
	v_cvt_pk_f16_f32 v6, v16, v17
	v_addc_co_u32_e32 v15, vcc, 0, v13, vcc
	ds_write2st64_b64 v0, v[4:5], v[6:7] offset0:72 offset1:76
	v_add_co_u32_e32 v68, vcc, s4, v12
	global_load_dwordx4 v[4:7], v[12:13], off sc0 sc1 nt
	global_load_dwordx4 v[8:11], v[14:15], off sc0 sc1 nt
	v_addc_co_u32_e32 v69, vcc, 0, v13, vcc
	s_add_i32 s0, s2, 0x240
	v_add_co_u32_e32 v70, vcc, s5, v12
	s_and_b32 s0, s0, 0x3c0
	s_nop 0
	v_addc_co_u32_e32 v71, vcc, 0, v13, vcc
	global_load_dwordx4 v[12:15], v[68:69], off sc0 sc1 nt
	global_load_dwordx4 v[16:19], v[70:71], off sc0 sc1 nt
	s_waitcnt vmcnt(15)
	v_cvt_pk_f16_f32 v23, v22, v23
	v_cvt_pk_f16_f32 v22, v20, v21
	s_waitcnt vmcnt(14)
	v_cvt_pk_f16_f32 v21, v26, v27
	v_cvt_pk_f16_f32 v20, v24, v25
	s_lshl_b32 s0, s0, 2
	s_waitcnt lgkmcnt(0)
	v_add_u32_e32 v171, 1, v171
	ds_write_b32 v169, v171
	ds_write2st64_b64 v0, v[22:23], v[20:21] offset0:80 offset1:84
	s_waitcnt vmcnt(13)
	v_cvt_pk_f16_f32 v20, v28, v29
	v_lshl_add_u64 v[28:29], v[2:3], 0, s[0:1]
	v_cvt_pk_f16_f32 v21, v30, v31
	v_add_co_u32_e32 v30, vcc, s3, v28
	s_waitcnt vmcnt(12)
	v_cvt_pk_f16_f32 v23, v34, v35
	v_cvt_pk_f16_f32 v22, v32, v33
	v_addc_co_u32_e32 v31, vcc, 0, v29, vcc
	ds_write2st64_b64 v0, v[20:21], v[22:23] offset0:88 offset1:92
	v_add_co_u32_e32 v68, vcc, s4, v28
	global_load_dwordx4 v[20:23], v[28:29], off sc0 sc1 nt
	global_load_dwordx4 v[24:27], v[30:31], off sc0 sc1 nt
	v_addc_co_u32_e32 v69, vcc, 0, v29, vcc
	s_add_i32 s0, s2, 0x280
	v_add_co_u32_e32 v70, vcc, s5, v28
	s_and_b32 s0, s0, 0x3c0
	s_nop 0
	v_addc_co_u32_e32 v71, vcc, 0, v29, vcc
	global_load_dwordx4 v[28:31], v[68:69], off sc0 sc1 nt
	global_load_dwordx4 v[32:35], v[70:71], off sc0 sc1 nt
	s_waitcnt vmcnt(15)
	v_cvt_pk_f16_f32 v39, v38, v39
	v_cvt_pk_f16_f32 v38, v36, v37
	s_waitcnt vmcnt(14)
	v_cvt_pk_f16_f32 v37, v42, v43
	v_cvt_pk_f16_f32 v36, v40, v41
	s_lshl_b32 s0, s0, 2
	s_waitcnt lgkmcnt(0)
	v_add_u32_e32 v171, 1, v171
	ds_write_b32 v169, v171
	ds_write2st64_b64 v0, v[38:39], v[36:37] offset0:96 offset1:100
	s_waitcnt vmcnt(13)
	v_cvt_pk_f16_f32 v36, v44, v45
	v_lshl_add_u64 v[44:45], v[2:3], 0, s[0:1]
	v_cvt_pk_f16_f32 v37, v46, v47
	v_add_co_u32_e32 v46, vcc, s3, v44
	s_waitcnt vmcnt(12)
	v_cvt_pk_f16_f32 v39, v50, v51
	v_cvt_pk_f16_f32 v38, v48, v49
	v_addc_co_u32_e32 v47, vcc, 0, v45, vcc
	ds_write2st64_b64 v0, v[36:37], v[38:39] offset0:104 offset1:108
	v_add_co_u32_e32 v68, vcc, s4, v44
	global_load_dwordx4 v[36:39], v[44:45], off sc0 sc1 nt
	global_load_dwordx4 v[40:43], v[46:47], off sc0 sc1 nt
	v_addc_co_u32_e32 v69, vcc, 0, v45, vcc
	v_add_co_u32_e32 v70, vcc, s5, v44
	s_add_i32 s0, s2, 0x2c0
	s_nop 0
	v_addc_co_u32_e32 v71, vcc, 0, v45, vcc
	global_load_dwordx4 v[44:47], v[68:69], off sc0 sc1 nt
	global_load_dwordx4 v[48:51], v[70:71], off sc0 sc1 nt
	s_and_b32 s0, s0, 0x3c0
	s_waitcnt vmcnt(15)
	v_cvt_pk_f16_f32 v55, v54, v55
	v_cvt_pk_f16_f32 v54, v52, v53
	s_waitcnt vmcnt(14)
	v_cvt_pk_f16_f32 v53, v58, v59
	v_cvt_pk_f16_f32 v52, v56, v57
	s_lshl_b32 s0, s0, 2
	s_waitcnt lgkmcnt(0)
	v_add_u32_e32 v171, 1, v171
	ds_write_b32 v169, v171
	ds_write2st64_b64 v0, v[54:55], v[52:53] offset0:112 offset1:116
	s_waitcnt vmcnt(13)
	v_cvt_pk_f16_f32 v53, v62, v63
	v_cvt_pk_f16_f32 v52, v60, v61
	s_waitcnt vmcnt(12)
	v_cvt_pk_f16_f32 v55, v66, v67
	v_cvt_pk_f16_f32 v54, v64, v65
	v_lshl_add_u64 v[60:61], v[2:3], 0, s[0:1]
	ds_write2st64_b64 v0, v[52:53], v[54:55] offset0:120 offset1:124
	v_add_co_u32_e32 v62, vcc, s3, v60
	s_add_i32 s0, s2, 0x300
	s_nop 0
	v_addc_co_u32_e32 v63, vcc, 0, v61, vcc
	global_load_dwordx4 v[52:55], v[60:61], off sc0 sc1 nt
	global_load_dwordx4 v[56:59], v[62:63], off sc0 sc1 nt
	v_add_co_u32_e32 v68, vcc, s4, v60
	s_waitcnt vmcnt(13)
	v_cvt_pk_f16_f32 v7, v6, v7
	v_addc_co_u32_e32 v69, vcc, 0, v61, vcc
	v_add_co_u32_e32 v70, vcc, s5, v60
	v_cvt_pk_f16_f32 v6, v4, v5
	s_and_b32 s0, s0, 0x3c0
	v_addc_co_u32_e32 v71, vcc, 0, v61, vcc
	global_load_dwordx4 v[60:63], v[68:69], off sc0 sc1 nt
	global_load_dwordx4 v[64:67], v[70:71], off sc0 sc1 nt
	s_waitcnt lgkmcnt(0)
	v_add_u32_e32 v171, 1, v171
	ds_write_b32 v169, v171
	ds_write_b64 v1, v[6:7]
	s_waitcnt vmcnt(14)
	v_cvt_pk_f16_f32 v5, v10, v11
	v_cvt_pk_f16_f32 v4, v8, v9
	v_add_u32_e32 v1, 0x10800, v0
	s_lshl_b32 s0, s0, 2
	ds_write_b64 v1, v[4:5]
	s_waitcnt vmcnt(13)
	v_cvt_pk_f16_f32 v4, v12, v13
	v_lshl_add_u64 v[12:13], v[2:3], 0, s[0:1]
	v_cvt_pk_f16_f32 v5, v14, v15
	v_add_co_u32_e32 v14, vcc, s3, v12
	v_add_u32_e32 v1, 0x11000, v0
	s_nop 0
	v_addc_co_u32_e32 v15, vcc, 0, v13, vcc
	v_add_co_u32_e32 v68, vcc, s4, v12
	ds_write_b64 v1, v[4:5]
	s_waitcnt vmcnt(12)
	v_cvt_pk_f16_f32 v5, v18, v19
	v_cvt_pk_f16_f32 v4, v16, v17
	v_add_u32_e32 v1, 0x11800, v0
	v_addc_co_u32_e32 v69, vcc, 0, v13, vcc
	s_add_i32 s0, s2, 0x340
	ds_write_b64 v1, v[4:5]
	v_add_co_u32_e32 v70, vcc, s5, v12
	s_waitcnt vmcnt(11)
	v_cvt_pk_f16_f32 v23, v22, v23
	v_cvt_pk_f16_f32 v22, v20, v21
	v_add_u32_e32 v1, 0x12000, v0
	s_and_b32 s0, s0, 0x3c0
	global_load_dwordx4 v[4:7], v[12:13], off sc0 sc1 nt
	global_load_dwordx4 v[8:11], v[14:15], off sc0 sc1 nt
	v_addc_co_u32_e32 v71, vcc, 0, v13, vcc
	global_load_dwordx4 v[12:15], v[68:69], off sc0 sc1 nt
	global_load_dwordx4 v[16:19], v[70:71], off sc0 sc1 nt
	s_waitcnt lgkmcnt(0)
	v_add_u32_e32 v171, 1, v171
	ds_write_b32 v169, v171
	ds_write_b64 v1, v[22:23]
	s_waitcnt vmcnt(14)
	v_cvt_pk_f16_f32 v21, v26, v27
	v_cvt_pk_f16_f32 v20, v24, v25
	v_add_u32_e32 v1, 0x12800, v0
	s_lshl_b32 s0, s0, 2
	ds_write_b64 v1, v[20:21]
	s_waitcnt vmcnt(13)
	v_cvt_pk_f16_f32 v20, v28, v29
	v_lshl_add_u64 v[28:29], v[2:3], 0, s[0:1]
	v_cvt_pk_f16_f32 v21, v30, v31
	v_add_co_u32_e32 v30, vcc, s3, v28
	v_add_u32_e32 v1, 0x13000, v0
	s_nop 0
	v_addc_co_u32_e32 v31, vcc, 0, v29, vcc
	v_add_co_u32_e32 v68, vcc, s4, v28
	ds_write_b64 v1, v[20:21]
	s_waitcnt vmcnt(12)
	v_cvt_pk_f16_f32 v21, v34, v35
	v_cvt_pk_f16_f32 v20, v32, v33
	v_add_u32_e32 v1, 0x13800, v0
	v_addc_co_u32_e32 v69, vcc, 0, v29, vcc
	s_add_i32 s0, s2, 0x380
	ds_write_b64 v1, v[20:21]
	v_add_co_u32_e32 v70, vcc, s5, v28
	s_waitcnt vmcnt(11)
	v_cvt_pk_f16_f32 v39, v38, v39
	v_cvt_pk_f16_f32 v38, v36, v37
	v_add_u32_e32 v1, 0x14000, v0
	s_and_b32 s0, s0, 0x3c0
	global_load_dwordx4 v[20:23], v[28:29], off sc0 sc1 nt
	global_load_dwordx4 v[24:27], v[30:31], off sc0 sc1 nt
	v_addc_co_u32_e32 v71, vcc, 0, v29, vcc
	global_load_dwordx4 v[28:31], v[68:69], off sc0 sc1 nt
	global_load_dwordx4 v[32:35], v[70:71], off sc0 sc1 nt
	s_waitcnt lgkmcnt(0)
	v_add_u32_e32 v171, 1, v171
	ds_write_b32 v169, v171
	ds_write_b64 v1, v[38:39]
	s_waitcnt vmcnt(14)
	v_cvt_pk_f16_f32 v37, v42, v43
	v_cvt_pk_f16_f32 v36, v40, v41
	v_add_u32_e32 v1, 0x14800, v0
	s_lshl_b32 s0, s0, 2
	ds_write_b64 v1, v[36:37]
	s_waitcnt vmcnt(13)
	v_cvt_pk_f16_f32 v36, v44, v45
	v_lshl_add_u64 v[44:45], v[2:3], 0, s[0:1]
	v_cvt_pk_f16_f32 v37, v46, v47
	v_add_co_u32_e32 v46, vcc, s3, v44
	s_addk_i32 s2, 0x3c0
	s_nop 0
	v_addc_co_u32_e32 v47, vcc, 0, v45, vcc
	v_add_co_u32_e32 v68, vcc, s4, v44
	v_add_u32_e32 v1, 0x15000, v0
	s_nop 0
	v_addc_co_u32_e32 v69, vcc, 0, v45, vcc
	s_and_b32 s0, s2, 0x3c0
	ds_write_b64 v1, v[36:37]
	s_waitcnt vmcnt(12)
	v_cvt_pk_f16_f32 v37, v50, v51
	v_cvt_pk_f16_f32 v36, v48, v49
	v_add_u32_e32 v1, 0x15800, v0
	v_add_co_u32_e32 v70, vcc, s5, v44
	s_lshl_b32 s0, s0, 2
	ds_write_b64 v1, v[36:37]
	v_addc_co_u32_e32 v71, vcc, 0, v45, vcc
	v_lshl_add_u64 v[2:3], v[2:3], 0, s[0:1]
	global_load_dwordx4 v[36:39], v[44:45], off sc0 sc1 nt
	global_load_dwordx4 v[40:43], v[46:47], off sc0 sc1 nt
	s_waitcnt vmcnt(13)
	v_cvt_pk_f16_f32 v55, v54, v55
	v_cvt_pk_f16_f32 v54, v52, v53
	s_waitcnt vmcnt(12)
	v_cvt_pk_f16_f32 v52, v56, v57
	v_add_co_u32_e32 v56, vcc, s3, v2
	v_add_u32_e32 v1, 0x16000, v0
	s_nop 0
	v_addc_co_u32_e32 v57, vcc, 0, v3, vcc
	global_load_dwordx4 v[44:47], v[68:69], off sc0 sc1 nt
	global_load_dwordx4 v[48:51], v[70:71], off sc0 sc1 nt
	s_waitcnt lgkmcnt(0)
	v_add_u32_e32 v171, 1, v171
	ds_write_b32 v169, v171
	ds_write_b64 v1, v[54:55]
	v_cvt_pk_f16_f32 v53, v58, v59
	v_add_u32_e32 v1, 0x16800, v0
	v_add_co_u32_e32 v68, vcc, s4, v2
	ds_write_b64 v1, v[52:53]
	global_load_dwordx4 v[52:55], v[2:3], off sc0 sc1 nt
	v_addc_co_u32_e32 v69, vcc, 0, v3, vcc
	global_load_dwordx4 v[56:59], v[56:57], off sc0 sc1 nt
	v_add_co_u32_e32 v2, vcc, s5, v2
	global_load_dwordx4 v[68:71], v[68:69], off sc0 sc1 nt
	s_nop 0
	v_addc_co_u32_e32 v3, vcc, 0, v3, vcc
	global_load_dwordx4 v[72:75], v[2:3], off sc0 sc1 nt
	s_waitcnt vmcnt(17)
	v_cvt_pk_f16_f32 v63, v62, v63
	v_cvt_pk_f16_f32 v62, v60, v61
	v_add_u32_e32 v1, 0x17000, v0
	ds_write_b64 v1, v[62:63]
	s_waitcnt vmcnt(16)
	v_cvt_pk_f16_f32 v3, v66, v67
	v_cvt_pk_f16_f32 v2, v64, v65
	v_add_u32_e32 v1, 0x17800, v0
	ds_write_b64 v1, v[2:3]
	s_waitcnt vmcnt(15)
	v_cvt_pk_f16_f32 v3, v6, v7
	v_cvt_pk_f16_f32 v2, v4, v5
	v_add_u32_e32 v1, 0x18000, v0
	s_waitcnt lgkmcnt(0)
	v_add_u32_e32 v171, 1, v171
	ds_write_b32 v169, v171
	ds_write_b64 v1, v[2:3]
	s_waitcnt vmcnt(14)
	v_cvt_pk_f16_f32 v3, v10, v11
	v_cvt_pk_f16_f32 v2, v8, v9
	v_add_u32_e32 v1, 0x18800, v0
	ds_write_b64 v1, v[2:3]
	s_waitcnt vmcnt(13)
	v_cvt_pk_f16_f32 v3, v14, v15
	v_cvt_pk_f16_f32 v2, v12, v13
	v_add_u32_e32 v1, 0x19000, v0
	ds_write_b64 v1, v[2:3]
	s_waitcnt vmcnt(12)
	v_cvt_pk_f16_f32 v3, v18, v19
	v_cvt_pk_f16_f32 v2, v16, v17
	v_add_u32_e32 v1, 0x19800, v0
	ds_write_b64 v1, v[2:3]
	s_waitcnt vmcnt(11)
	v_cvt_pk_f16_f32 v3, v22, v23
	v_cvt_pk_f16_f32 v2, v20, v21
	v_add_u32_e32 v1, 0x1a000, v0
	s_waitcnt lgkmcnt(0)
	v_add_u32_e32 v171, 1, v171
	ds_write_b32 v169, v171
	ds_write_b64 v1, v[2:3]
	s_waitcnt vmcnt(10)
	v_cvt_pk_f16_f32 v3, v26, v27
	v_cvt_pk_f16_f32 v2, v24, v25
	v_add_u32_e32 v1, 0x1a800, v0
	ds_write_b64 v1, v[2:3]
	s_waitcnt vmcnt(9)
	v_cvt_pk_f16_f32 v3, v30, v31
	v_cvt_pk_f16_f32 v2, v28, v29
	v_add_u32_e32 v1, 0x1b000, v0
	ds_write_b64 v1, v[2:3]
	s_waitcnt vmcnt(8)
	v_cvt_pk_f16_f32 v3, v34, v35
	v_cvt_pk_f16_f32 v2, v32, v33
	v_add_u32_e32 v1, 0x1b800, v0
	ds_write_b64 v1, v[2:3]
	v_add_u32_e32 v1, 0x1c000, v0
	s_waitcnt lgkmcnt(0)
	v_add_u32_e32 v171, 1, v171
	ds_write_b32 v169, v171
	s_waitcnt vmcnt(7)
	v_cvt_pk_f16_f32 v3, v38, v39
	v_cvt_pk_f16_f32 v2, v36, v37
	ds_write_b64 v1, v[2:3]
	s_waitcnt vmcnt(6)
	v_cvt_pk_f16_f32 v3, v42, v43
	v_cvt_pk_f16_f32 v2, v40, v41
	v_add_u32_e32 v1, 0x1c800, v0
	ds_write_b64 v1, v[2:3]
	v_add_u32_e32 v1, 0x1d000, v0
	s_waitcnt vmcnt(5)
	v_cvt_pk_f16_f32 v3, v46, v47
	v_cvt_pk_f16_f32 v2, v44, v45
	ds_write_b64 v1, v[2:3]
	s_waitcnt vmcnt(4)
	v_cvt_pk_f16_f32 v3, v50, v51
	v_cvt_pk_f16_f32 v2, v48, v49
	v_add_u32_e32 v1, 0x1d800, v0
	ds_write_b64 v1, v[2:3]
	v_add_u32_e32 v1, 0x1e000, v0
	s_waitcnt lgkmcnt(0)
	v_add_u32_e32 v171, 1, v171
	ds_write_b32 v169, v171
	s_waitcnt vmcnt(3)
	v_cvt_pk_f16_f32 v3, v54, v55
	v_cvt_pk_f16_f32 v2, v52, v53
	ds_write_b64 v1, v[2:3]
	s_waitcnt vmcnt(2)
	v_cvt_pk_f16_f32 v3, v58, v59
	v_cvt_pk_f16_f32 v2, v56, v57
	v_add_u32_e32 v1, 0x1e800, v0
	ds_write_b64 v1, v[2:3]
	s_waitcnt vmcnt(1)
	v_cvt_pk_f16_f32 v3, v70, v71
	v_cvt_pk_f16_f32 v2, v68, v69
	v_add_u32_e32 v1, 0x1f000, v0
	ds_write_b64 v1, v[2:3]
	s_waitcnt vmcnt(0)
	v_cvt_pk_f16_f32 v3, v74, v75
	v_cvt_pk_f16_f32 v2, v72, v73
	v_add_u32_e32 v0, 0x1f800, v0
	ds_write_b64 v0, v[2:3]
	s_waitcnt lgkmcnt(0)
	v_add_u32_e32 v171, 1, v171
	ds_write_b32 v169, v171
	s_waitcnt lgkmcnt(0)
	s_endpgm
